# GEMM K-loops (proj, out, up): first K-tile MFMAs write accumulators with C=0 instead of a 128-v_mov zeroing pass per tile
# speedup vs baseline: 1.0015x; 1.0015x over previous
.LBB0_234:
	s_ashr_i32 s21, s20, 31
	s_lshl_b64 s[0:1], s[20:21], 18
	s_add_u32 s24, s30, s0
	s_addc_u32 s25, s31, s1
	s_and_b64 s[0:1], s[40:41], exec
	s_cselect_b32 s21, s25, s7
	s_cselect_b32 s29, s24, s6
	s_ashr_i32 s23, s22, 31
	s_lshl_b64 s[0:1], s[22:23], 18
	s_add_u32 s26, s34, s0
	s_addc_u32 s27, s35, s1
	s_and_b64 s[0:1], s[40:41], exec
	s_cselect_b32 s23, s27, s5
	s_cselect_b32 s48, s26, s4
	s_add_u32 s0, s6, 0x20080
	s_addc_u32 s1, s7, 0
	s_add_u32 s49, s4, 0x100
	v_mov_b32_e32 v100, 0
	s_addc_u32 s50, s5, 0
	s_mov_b32 s51, -2
	s_mov_b64 s[56:57], 0x80
.LBB0_235:
	s_add_u32 s4, s0, 0xfffe0080
	s_addc_u32 s5, s1, -1
	s_add_i32 s52, 0, 0x10000
	s_cmp_eq_u32 s51, 4
	s_cselect_b32 s7, s21, s5
	s_cselect_b32 s6, s29, s4
	s_cselect_b32 s5, s23, s50
	s_cselect_b32 s4, s48, s49
	s_add_i32 s53, 0, 0x14000
	ds_read_b128 v[20:23], v192
	ds_read_b128 v[24:27], v249
	ds_read_b128 v[28:31], v192 offset:2048
	ds_read_b128 v[32:35], v249 offset:2048
	ds_read_b128 v[4:7], v192 offset:16384
	ds_read_b128 v[8:11], v249 offset:16384
	ds_read_b128 v[12:15], v192 offset:18432
	ds_read_b128 v[16:19], v249 offset:18432
	v_lshl_add_u64 v[234:235], s[0:1], 0, v[180:181]
	s_add_i32 m0, s37, 0xc000
	ds_read_b128 v[184:187], v193
	ds_read_b128 v[188:191], v250
	ds_read_b128 v[194:197], v193 offset:2048
	ds_read_b128 v[198:201], v250 offset:2048
	ds_read_b128 v[202:205], v193 offset:4096
	ds_read_b128 v[206:209], v250 offset:4096
	ds_read_b128 v[226:229], v193 offset:6144
	ds_read_b128 v[230:233], v250 offset:6144
	global_load_lds_dwordx4 v[234:235], off
	v_lshl_add_u64 v[234:235], s[0:1], 0, v[182:183]
	s_add_i32 m0, s37, 0xe000
	s_nop 0
	global_load_lds_dwordx4 v[234:235], off
	s_waitcnt vmcnt(8)
	s_waitcnt lgkmcnt(0)
	s_barrier
	s_setprio 1
	s_cmp_eq_u32 s51, -2
	s_cbranch_scc1 .LCZ0_0_z
	v_mfma_f32_16x16x128_f8f6f4 v[96:99], v[20:27], v[184:191], v[96:99]
	v_mfma_f32_16x16x128_f8f6f4 v[92:95], v[28:35], v[184:191], v[92:95]
	v_mfma_f32_16x16x128_f8f6f4 v[88:91], v[20:27], v[194:201], v[88:91]
	v_mfma_f32_16x16x128_f8f6f4 v[84:87], v[28:35], v[194:201], v[84:87]
	v_mfma_f32_16x16x128_f8f6f4 v[80:83], v[20:27], v[202:209], v[80:83]
	v_mfma_f32_16x16x128_f8f6f4 v[76:79], v[28:35], v[202:209], v[76:79]
	v_mfma_f32_16x16x128_f8f6f4 v[72:75], v[20:27], v[226:233], v[72:75]
	v_mfma_f32_16x16x128_f8f6f4 v[68:71], v[28:35], v[226:233], v[68:71]
	v_mfma_f32_16x16x128_f8f6f4 v[160:163], v[4:11], v[184:191], v[160:163]
	v_mfma_f32_16x16x128_f8f6f4 v[156:159], v[12:19], v[184:191], v[156:159]
	v_mfma_f32_16x16x128_f8f6f4 v[152:155], v[4:11], v[194:201], v[152:155]
	v_mfma_f32_16x16x128_f8f6f4 v[148:151], v[12:19], v[194:201], v[148:151]
	v_mfma_f32_16x16x128_f8f6f4 v[144:147], v[4:11], v[202:209], v[144:147]
	v_mfma_f32_16x16x128_f8f6f4 v[140:143], v[12:19], v[202:209], v[140:143]
	v_mfma_f32_16x16x128_f8f6f4 v[136:139], v[4:11], v[226:233], v[136:139]
	v_mfma_f32_16x16x128_f8f6f4 v[132:135], v[12:19], v[226:233], v[132:135]
	s_branch .LCZ0_0_j
.LCZ0_0_z:
	v_mfma_f32_16x16x128_f8f6f4 v[96:99], v[20:27], v[184:191], 0
	v_mfma_f32_16x16x128_f8f6f4 v[92:95], v[28:35], v[184:191], 0
	v_mfma_f32_16x16x128_f8f6f4 v[88:91], v[20:27], v[194:201], 0
	v_mfma_f32_16x16x128_f8f6f4 v[84:87], v[28:35], v[194:201], 0
	v_mfma_f32_16x16x128_f8f6f4 v[80:83], v[20:27], v[202:209], 0
	v_mfma_f32_16x16x128_f8f6f4 v[76:79], v[28:35], v[202:209], 0
	v_mfma_f32_16x16x128_f8f6f4 v[72:75], v[20:27], v[226:233], 0
	v_mfma_f32_16x16x128_f8f6f4 v[68:71], v[28:35], v[226:233], 0
	v_mfma_f32_16x16x128_f8f6f4 v[160:163], v[4:11], v[184:191], 0
	v_mfma_f32_16x16x128_f8f6f4 v[156:159], v[12:19], v[184:191], 0
	v_mfma_f32_16x16x128_f8f6f4 v[152:155], v[4:11], v[194:201], 0
	v_mfma_f32_16x16x128_f8f6f4 v[148:151], v[12:19], v[194:201], 0
	v_mfma_f32_16x16x128_f8f6f4 v[144:147], v[4:11], v[202:209], 0
	v_mfma_f32_16x16x128_f8f6f4 v[140:143], v[12:19], v[202:209], 0
	v_mfma_f32_16x16x128_f8f6f4 v[136:139], v[4:11], v[226:233], 0
	v_mfma_f32_16x16x128_f8f6f4 v[132:135], v[12:19], v[226:233], 0
.LCZ0_0_j:
	s_setprio 0
	s_barrier
	s_add_i32 s52, s52, s36
	v_lshl_add_u64 v[184:185], s[4:5], 0, v[176:177]
	s_mov_b32 m0, s52
	ds_read_b128 v[194:197], v193 offset:16384
	ds_read_b128 v[198:201], v250 offset:16384
	ds_read_b128 v[202:205], v193 offset:18432
	ds_read_b128 v[206:209], v250 offset:18432
	ds_read_b128 v[226:229], v193 offset:20480
	ds_read_b128 v[230:233], v250 offset:20480
	ds_read_b128 v[234:237], v193 offset:22528
	ds_read_b128 v[238:241], v250 offset:22528
	global_load_lds_dwordx4 v[184:185], off
	s_add_i32 m0, s52, 0x2000
	s_add_u32 s54, s4, 0x20000
	v_lshl_add_u64 v[186:187], s[4:5], 0, v[172:173]
	s_addc_u32 s55, s5, 0
	s_add_i32 s52, s53, s36
	global_load_lds_dwordx4 v[186:187], off
	v_lshl_add_u64 v[188:189], s[54:55], 0, v[176:177]
	s_mov_b32 m0, s52
	v_lshl_add_u64 v[190:191], s[6:7], 0, v[174:175]
	global_load_lds_dwordx4 v[188:189], off
	v_lshl_add_u64 v[188:189], s[54:55], 0, v[172:173]
	s_add_i32 m0, s52, 0x2000
	s_nop 0
	global_load_lds_dwordx4 v[188:189], off
	v_lshl_add_u64 v[188:189], s[6:7], 0, v[178:179]
	s_mov_b32 m0, s37
	s_nop 0
	global_load_lds_dwordx4 v[188:189], off
	s_mov_b32 m0, s38
	s_nop 0
	global_load_lds_dwordx4 v[190:191], off
	s_waitcnt vmcnt(8)
	s_waitcnt lgkmcnt(0)
	s_barrier
	s_setprio 1
	s_cmp_eq_u32 s51, -2
	s_cbranch_scc1 .LCZ0_1_z
	v_mfma_f32_16x16x128_f8f6f4 v[64:67], v[20:27], v[194:201], v[64:67]
	v_mfma_f32_16x16x128_f8f6f4 v[60:63], v[28:35], v[194:201], v[60:63]
	v_mfma_f32_16x16x128_f8f6f4 v[56:59], v[20:27], v[202:209], v[56:59]
	v_mfma_f32_16x16x128_f8f6f4 v[52:55], v[28:35], v[202:209], v[52:55]
	v_mfma_f32_16x16x128_f8f6f4 v[48:51], v[20:27], v[226:233], v[48:51]
	v_mfma_f32_16x16x128_f8f6f4 v[44:47], v[28:35], v[226:233], v[44:47]
	v_mfma_f32_16x16x128_f8f6f4 v[40:43], v[20:27], v[234:241], v[40:43]
	v_mfma_f32_16x16x128_f8f6f4 v[36:39], v[28:35], v[234:241], v[36:39]
	v_mfma_f32_16x16x128_f8f6f4 v[128:131], v[4:11], v[194:201], v[128:131]
	v_mfma_f32_16x16x128_f8f6f4 v[124:127], v[12:19], v[194:201], v[124:127]
	v_mfma_f32_16x16x128_f8f6f4 v[120:123], v[4:11], v[202:209], v[120:123]
	v_mfma_f32_16x16x128_f8f6f4 v[116:119], v[12:19], v[202:209], v[116:119]
	v_mfma_f32_16x16x128_f8f6f4 v[112:115], v[4:11], v[226:233], v[112:115]
	v_mfma_f32_16x16x128_f8f6f4 v[108:111], v[12:19], v[226:233], v[108:111]
	v_mfma_f32_16x16x128_f8f6f4 v[104:107], v[4:11], v[234:241], v[104:107]
	v_mfma_f32_16x16x128_f8f6f4 v[100:103], v[12:19], v[234:241], v[100:103]
	s_branch .LCZ0_1_j
.LCZ0_1_z:
	v_mfma_f32_16x16x128_f8f6f4 v[64:67], v[20:27], v[194:201], 0
	v_mfma_f32_16x16x128_f8f6f4 v[60:63], v[28:35], v[194:201], 0
	v_mfma_f32_16x16x128_f8f6f4 v[56:59], v[20:27], v[202:209], 0
	v_mfma_f32_16x16x128_f8f6f4 v[52:55], v[28:35], v[202:209], 0
	v_mfma_f32_16x16x128_f8f6f4 v[48:51], v[20:27], v[226:233], 0
	v_mfma_f32_16x16x128_f8f6f4 v[44:47], v[28:35], v[226:233], 0
	v_mfma_f32_16x16x128_f8f6f4 v[40:43], v[20:27], v[234:241], 0
	v_mfma_f32_16x16x128_f8f6f4 v[36:39], v[28:35], v[234:241], 0
	v_mfma_f32_16x16x128_f8f6f4 v[128:131], v[4:11], v[194:201], 0
	v_mfma_f32_16x16x128_f8f6f4 v[124:127], v[12:19], v[194:201], 0
	v_mfma_f32_16x16x128_f8f6f4 v[120:123], v[4:11], v[202:209], 0
	v_mfma_f32_16x16x128_f8f6f4 v[116:119], v[12:19], v[202:209], 0
	v_mfma_f32_16x16x128_f8f6f4 v[112:115], v[4:11], v[226:233], 0
	v_mfma_f32_16x16x128_f8f6f4 v[108:111], v[12:19], v[226:233], 0
	v_mfma_f32_16x16x128_f8f6f4 v[104:107], v[4:11], v[234:241], 0
	v_mfma_f32_16x16x128_f8f6f4 v[100:103], v[12:19], v[234:241], 0
.LCZ0_1_j:
	s_setprio 0
	s_barrier
	s_add_i32 s52, 0, 0x18000
	s_add_i32 s53, 0, 0x1c000
	ds_read_b128 v[4:7], v192 offset:32768
	ds_read_b128 v[8:11], v249 offset:32768
	ds_read_b128 v[12:15], v192 offset:34816
	ds_read_b128 v[16:19], v249 offset:34816
	ds_read_b128 v[20:23], v192 offset:49152
	ds_read_b128 v[24:27], v249 offset:49152
	ds_read_b128 v[28:31], v192 offset:51200
	ds_read_b128 v[32:35], v249 offset:51200
	s_add_u32 s6, s6, 0x20000
	s_addc_u32 s7, s7, 0
	s_mov_b32 m0, s39
	v_lshl_add_u64 v[242:243], s[6:7], 0, v[178:179]
	ds_read_b128 v[194:197], v193 offset:32768
	ds_read_b128 v[198:201], v250 offset:32768
	ds_read_b128 v[202:205], v193 offset:34816
	ds_read_b128 v[206:209], v250 offset:34816
	ds_read_b128 v[226:229], v193 offset:36864
	ds_read_b128 v[230:233], v250 offset:36864
	ds_read_b128 v[234:237], v193 offset:38912
	ds_read_b128 v[238:241], v250 offset:38912
	global_load_lds_dwordx4 v[242:243], off
	v_lshl_add_u64 v[242:243], s[6:7], 0, v[174:175]
	s_mov_b32 m0, s42
	s_nop 0
	global_load_lds_dwordx4 v[242:243], off
	s_waitcnt vmcnt(8)
	s_waitcnt lgkmcnt(0)
	s_barrier
	s_setprio 1
	v_mfma_f32_16x16x128_f8f6f4 v[96:99], v[4:11], v[194:201], v[96:99]
	v_mfma_f32_16x16x128_f8f6f4 v[92:95], v[12:19], v[194:201], v[92:95]
	v_mfma_f32_16x16x128_f8f6f4 v[88:91], v[4:11], v[202:209], v[88:91]
	v_mfma_f32_16x16x128_f8f6f4 v[84:87], v[12:19], v[202:209], v[84:87]
	v_mfma_f32_16x16x128_f8f6f4 v[80:83], v[4:11], v[226:233], v[80:83]
	v_mfma_f32_16x16x128_f8f6f4 v[76:79], v[12:19], v[226:233], v[76:79]
	v_mfma_f32_16x16x128_f8f6f4 v[72:75], v[4:11], v[234:241], v[72:75]
	v_mfma_f32_16x16x128_f8f6f4 v[68:71], v[12:19], v[234:241], v[68:71]
	v_mfma_f32_16x16x128_f8f6f4 v[160:163], v[20:27], v[194:201], v[160:163]
	v_mfma_f32_16x16x128_f8f6f4 v[156:159], v[28:35], v[194:201], v[156:159]
	v_mfma_f32_16x16x128_f8f6f4 v[152:155], v[20:27], v[202:209], v[152:155]
	v_mfma_f32_16x16x128_f8f6f4 v[148:151], v[28:35], v[202:209], v[148:151]
	v_mfma_f32_16x16x128_f8f6f4 v[144:147], v[20:27], v[226:233], v[144:147]
	v_mfma_f32_16x16x128_f8f6f4 v[140:143], v[28:35], v[226:233], v[140:143]
	v_mfma_f32_16x16x128_f8f6f4 v[136:139], v[20:27], v[234:241], v[136:139]
	v_mfma_f32_16x16x128_f8f6f4 v[132:135], v[28:35], v[234:241], v[132:135]
	s_setprio 0
	s_barrier
	s_add_i32 s6, s52, s36
	v_lshl_add_u64 v[184:185], v[184:185], 0, s[56:57]
	s_mov_b32 m0, s6
	ds_read_b128 v[194:197], v193 offset:49152
	ds_read_b128 v[198:201], v250 offset:49152
	ds_read_b128 v[202:205], v193 offset:51200
	ds_read_b128 v[206:209], v250 offset:51200
	ds_read_b128 v[226:229], v193 offset:53248
	ds_read_b128 v[230:233], v250 offset:53248
	ds_read_b128 v[234:237], v193 offset:55296
	ds_read_b128 v[238:241], v250 offset:55296
	global_load_lds_dwordx4 v[184:185], off
	s_add_i32 m0, s6, 0x2000
	s_add_u32 s4, s4, 0x20080
	v_lshl_add_u64 v[184:185], v[186:187], 0, s[56:57]
	s_addc_u32 s5, s5, 0
	s_add_i32 s6, s53, s36
	global_load_lds_dwordx4 v[184:185], off
	v_lshl_add_u64 v[184:185], s[4:5], 0, v[176:177]
	s_mov_b32 m0, s6
	s_nop 0
	global_load_lds_dwordx4 v[184:185], off
	v_lshl_add_u64 v[184:185], s[4:5], 0, v[172:173]
	s_add_i32 m0, s6, 0x2000
	s_nop 0
	global_load_lds_dwordx4 v[184:185], off
	v_lshl_add_u64 v[184:185], v[188:189], 0, s[56:57]
	s_mov_b32 m0, s45
	s_nop 0
	global_load_lds_dwordx4 v[184:185], off
	v_lshl_add_u64 v[184:185], v[190:191], 0, s[56:57]
	s_mov_b32 m0, s46
	s_nop 0
	global_load_lds_dwordx4 v[184:185], off
	s_waitcnt vmcnt(8)
	s_waitcnt lgkmcnt(0)
	s_barrier
	s_setprio 1
	v_mfma_f32_16x16x128_f8f6f4 v[64:67], v[4:11], v[194:201], v[64:67]
	v_mfma_f32_16x16x128_f8f6f4 v[60:63], v[12:19], v[194:201], v[60:63]
	v_mfma_f32_16x16x128_f8f6f4 v[56:59], v[4:11], v[202:209], v[56:59]
	v_mfma_f32_16x16x128_f8f6f4 v[52:55], v[12:19], v[202:209], v[52:55]
	v_mfma_f32_16x16x128_f8f6f4 v[48:51], v[4:11], v[226:233], v[48:51]
	v_mfma_f32_16x16x128_f8f6f4 v[44:47], v[12:19], v[226:233], v[44:47]
	v_mfma_f32_16x16x128_f8f6f4 v[40:43], v[4:11], v[234:241], v[40:43]
	v_mfma_f32_16x16x128_f8f6f4 v[36:39], v[12:19], v[234:241], v[36:39]
	v_mfma_f32_16x16x128_f8f6f4 v[128:131], v[20:27], v[194:201], v[128:131]
	v_mfma_f32_16x16x128_f8f6f4 v[124:127], v[28:35], v[194:201], v[124:127]
	v_mfma_f32_16x16x128_f8f6f4 v[120:123], v[20:27], v[202:209], v[120:123]
	v_mfma_f32_16x16x128_f8f6f4 v[116:119], v[28:35], v[202:209], v[116:119]
	v_mfma_f32_16x16x128_f8f6f4 v[112:115], v[20:27], v[226:233], v[112:115]
	v_mfma_f32_16x16x128_f8f6f4 v[108:111], v[28:35], v[226:233], v[108:111]
	v_mfma_f32_16x16x128_f8f6f4 v[104:107], v[20:27], v[234:241], v[104:107]
	v_mfma_f32_16x16x128_f8f6f4 v[100:103], v[28:35], v[234:241], v[100:103]
	s_setprio 0
	s_barrier
	s_add_i32 s51, s51, 2
	s_add_u32 s0, s0, 0x100
	s_addc_u32 s1, s1, 0
	s_add_u32 s49, s49, 0x100
	s_addc_u32 s50, s50, 0
	s_cmp_gt_u32 s51, 5
	s_cbranch_scc0 .LBB0_235
	s_and_b64 vcc, exec, s[18:19]
	s_cbranch_vccz .LBB0_238
	s_barrier

.LBB0_701:
	s_ashr_i32 s13, s12, 31
	s_lshl_b64 s[16:17], s[12:13], 18
	s_add_u32 s16, s24, s16
	s_addc_u32 s17, s25, s17
	s_and_b64 s[0:1], s[0:1], exec
	s_cselect_b32 s13, s17, s19
	s_cselect_b32 s43, s16, s18
	s_add_u32 s0, s20, 0x130080
	s_addc_u32 s1, s21, 0
	s_add_u32 s44, s18, 0x100
	v_mov_b32_e32 v36, 0
	s_addc_u32 s45, s19, 0
	s_mov_b32 s46, -2
	s_mov_b64 s[52:53], 0x80
.LBB0_702:
	s_add_u32 s18, s0, 0xffed0080
	s_addc_u32 s19, s1, -1
	s_add_i32 s47, 0, 0x10000
	s_cmp_eq_u32 s46, 4
	s_cselect_b32 s21, s15, s19
	s_cselect_b32 s20, s14, s18
	s_cselect_b32 s19, s13, s45
	s_cselect_b32 s18, s43, s44
	s_add_i32 s48, 0, 0x14000
	ds_read_b128 v[20:23], v226
	ds_read_b128 v[24:27], v245
	ds_read_b128 v[28:31], v226 offset:2048
	ds_read_b128 v[32:35], v245 offset:2048
	ds_read_b128 v[4:7], v226 offset:16384
	ds_read_b128 v[8:11], v245 offset:16384
	ds_read_b128 v[12:15], v226 offset:18432
	ds_read_b128 v[16:19], v245 offset:18432
	v_lshl_add_u64 v[164:165], s[0:1], 0, v[180:181]
	s_add_i32 m0, s27, 0xc000
	ds_read_b128 v[184:187], v227
	ds_read_b128 v[188:191], v246
	ds_read_b128 v[192:195], v227 offset:2048
	ds_read_b128 v[196:199], v246 offset:2048
	ds_read_b128 v[200:203], v227 offset:4096
	ds_read_b128 v[204:207], v246 offset:4096
	ds_read_b128 v[228:231], v227 offset:6144
	ds_read_b128 v[232:235], v246 offset:6144
	global_load_lds_dwordx4 v[164:165], off
	v_lshl_add_u64 v[164:165], s[0:1], 0, v[182:183]
	s_add_i32 m0, s27, 0xe000
	s_nop 0
	global_load_lds_dwordx4 v[164:165], off
	s_waitcnt vmcnt(8)
	s_waitcnt lgkmcnt(0)
	s_barrier
	s_setprio 1
	s_cmp_eq_u32 s46, -2
	s_cbranch_scc1 .LCZ1_0_z
	v_mfma_f32_16x16x128_f8f6f4 v[160:163], v[20:27], v[184:191], v[160:163]
	v_mfma_f32_16x16x128_f8f6f4 v[156:159], v[28:35], v[184:191], v[156:159]
	v_mfma_f32_16x16x128_f8f6f4 v[144:147], v[20:27], v[192:199], v[144:147]
	v_mfma_f32_16x16x128_f8f6f4 v[140:143], v[28:35], v[192:199], v[140:143]
	v_mfma_f32_16x16x128_f8f6f4 v[128:131], v[20:27], v[200:207], v[128:131]
	v_mfma_f32_16x16x128_f8f6f4 v[124:127], v[28:35], v[200:207], v[124:127]
	v_mfma_f32_16x16x128_f8f6f4 v[112:115], v[20:27], v[228:235], v[112:115]
	v_mfma_f32_16x16x128_f8f6f4 v[108:111], v[28:35], v[228:235], v[108:111]
	v_mfma_f32_16x16x128_f8f6f4 v[152:155], v[4:11], v[184:191], v[152:155]
	v_mfma_f32_16x16x128_f8f6f4 v[148:151], v[12:19], v[184:191], v[148:151]
	v_mfma_f32_16x16x128_f8f6f4 v[136:139], v[4:11], v[192:199], v[136:139]
	v_mfma_f32_16x16x128_f8f6f4 v[132:135], v[12:19], v[192:199], v[132:135]
	v_mfma_f32_16x16x128_f8f6f4 v[120:123], v[4:11], v[200:207], v[120:123]
	v_mfma_f32_16x16x128_f8f6f4 v[116:119], v[12:19], v[200:207], v[116:119]
	v_mfma_f32_16x16x128_f8f6f4 v[104:107], v[4:11], v[228:235], v[104:107]
	v_mfma_f32_16x16x128_f8f6f4 v[100:103], v[12:19], v[228:235], v[100:103]
	s_branch .LCZ1_0_j
.LCZ1_0_z:
	v_mfma_f32_16x16x128_f8f6f4 v[160:163], v[20:27], v[184:191], 0
	v_mfma_f32_16x16x128_f8f6f4 v[156:159], v[28:35], v[184:191], 0
	v_mfma_f32_16x16x128_f8f6f4 v[144:147], v[20:27], v[192:199], 0
	v_mfma_f32_16x16x128_f8f6f4 v[140:143], v[28:35], v[192:199], 0
	v_mfma_f32_16x16x128_f8f6f4 v[128:131], v[20:27], v[200:207], 0
	v_mfma_f32_16x16x128_f8f6f4 v[124:127], v[28:35], v[200:207], 0
	v_mfma_f32_16x16x128_f8f6f4 v[112:115], v[20:27], v[228:235], 0
	v_mfma_f32_16x16x128_f8f6f4 v[108:111], v[28:35], v[228:235], 0
	v_mfma_f32_16x16x128_f8f6f4 v[152:155], v[4:11], v[184:191], 0
	v_mfma_f32_16x16x128_f8f6f4 v[148:151], v[12:19], v[184:191], 0
	v_mfma_f32_16x16x128_f8f6f4 v[136:139], v[4:11], v[192:199], 0
	v_mfma_f32_16x16x128_f8f6f4 v[132:135], v[12:19], v[192:199], 0
	v_mfma_f32_16x16x128_f8f6f4 v[120:123], v[4:11], v[200:207], 0
	v_mfma_f32_16x16x128_f8f6f4 v[116:119], v[12:19], v[200:207], 0
	v_mfma_f32_16x16x128_f8f6f4 v[104:107], v[4:11], v[228:235], 0
	v_mfma_f32_16x16x128_f8f6f4 v[100:103], v[12:19], v[228:235], 0
.LCZ1_0_j:
	s_setprio 0
	s_barrier
	s_add_i32 s47, s47, s26
	v_lshl_add_u64 v[184:185], s[18:19], 0, v[176:177]
	s_mov_b32 m0, s47
	ds_read_b128 v[192:195], v227 offset:16384
	ds_read_b128 v[196:199], v246 offset:16384
	ds_read_b128 v[200:203], v227 offset:18432
	ds_read_b128 v[204:207], v246 offset:18432
	ds_read_b128 v[228:231], v227 offset:20480
	ds_read_b128 v[232:235], v246 offset:20480
	ds_read_b128 v[236:239], v227 offset:22528
	ds_read_b128 v[240:243], v246 offset:22528
	global_load_lds_dwordx4 v[184:185], off
	s_add_i32 m0, s47, 0x2000
	s_add_u32 s50, s18, 0x20000
	v_lshl_add_u64 v[186:187], s[18:19], 0, v[172:173]
	s_addc_u32 s51, s19, 0
	s_add_i32 s47, s48, s26
	global_load_lds_dwordx4 v[186:187], off
	v_lshl_add_u64 v[164:165], s[50:51], 0, v[176:177]
	s_mov_b32 m0, s47
	v_lshl_add_u64 v[188:189], s[20:21], 0, v[178:179]
	global_load_lds_dwordx4 v[164:165], off
	v_lshl_add_u64 v[164:165], s[50:51], 0, v[172:173]
	s_add_i32 m0, s47, 0x2000
	v_lshl_add_u64 v[190:191], s[20:21], 0, v[174:175]
	global_load_lds_dwordx4 v[164:165], off
	s_mov_b32 m0, s27
	s_nop 0
	global_load_lds_dwordx4 v[188:189], off
	s_mov_b32 m0, s28
	s_nop 0
	global_load_lds_dwordx4 v[190:191], off
	s_waitcnt vmcnt(8)
	s_waitcnt lgkmcnt(0)
	s_barrier
	s_setprio 1
	s_cmp_eq_u32 s46, -2
	s_cbranch_scc1 .LCZ1_1_z
	v_mfma_f32_16x16x128_f8f6f4 v[96:99], v[20:27], v[192:199], v[96:99]
	v_mfma_f32_16x16x128_f8f6f4 v[92:95], v[28:35], v[192:199], v[92:95]
	v_mfma_f32_16x16x128_f8f6f4 v[80:83], v[20:27], v[200:207], v[80:83]
	v_mfma_f32_16x16x128_f8f6f4 v[76:79], v[28:35], v[200:207], v[76:79]
	v_mfma_f32_16x16x128_f8f6f4 v[64:67], v[20:27], v[228:235], v[64:67]
	v_mfma_f32_16x16x128_f8f6f4 v[60:63], v[28:35], v[228:235], v[60:63]
	v_mfma_f32_16x16x128_f8f6f4 v[48:51], v[20:27], v[236:243], v[48:51]
	v_mfma_f32_16x16x128_f8f6f4 v[44:47], v[28:35], v[236:243], v[44:47]
	v_mfma_f32_16x16x128_f8f6f4 v[88:91], v[4:11], v[192:199], v[88:91]
	v_mfma_f32_16x16x128_f8f6f4 v[84:87], v[12:19], v[192:199], v[84:87]
	v_mfma_f32_16x16x128_f8f6f4 v[72:75], v[4:11], v[200:207], v[72:75]
	v_mfma_f32_16x16x128_f8f6f4 v[68:71], v[12:19], v[200:207], v[68:71]
	v_mfma_f32_16x16x128_f8f6f4 v[56:59], v[4:11], v[228:235], v[56:59]
	v_mfma_f32_16x16x128_f8f6f4 v[52:55], v[12:19], v[228:235], v[52:55]
	v_mfma_f32_16x16x128_f8f6f4 v[40:43], v[4:11], v[236:243], v[40:43]
	v_mfma_f32_16x16x128_f8f6f4 v[36:39], v[12:19], v[236:243], v[36:39]
	s_branch .LCZ1_1_j
.LCZ1_1_z:
	v_mfma_f32_16x16x128_f8f6f4 v[96:99], v[20:27], v[192:199], 0
	v_mfma_f32_16x16x128_f8f6f4 v[92:95], v[28:35], v[192:199], 0
	v_mfma_f32_16x16x128_f8f6f4 v[80:83], v[20:27], v[200:207], 0
	v_mfma_f32_16x16x128_f8f6f4 v[76:79], v[28:35], v[200:207], 0
	v_mfma_f32_16x16x128_f8f6f4 v[64:67], v[20:27], v[228:235], 0
	v_mfma_f32_16x16x128_f8f6f4 v[60:63], v[28:35], v[228:235], 0
	v_mfma_f32_16x16x128_f8f6f4 v[48:51], v[20:27], v[236:243], 0
	v_mfma_f32_16x16x128_f8f6f4 v[44:47], v[28:35], v[236:243], 0
	v_mfma_f32_16x16x128_f8f6f4 v[88:91], v[4:11], v[192:199], 0
	v_mfma_f32_16x16x128_f8f6f4 v[84:87], v[12:19], v[192:199], 0
	v_mfma_f32_16x16x128_f8f6f4 v[72:75], v[4:11], v[200:207], 0
	v_mfma_f32_16x16x128_f8f6f4 v[68:71], v[12:19], v[200:207], 0
	v_mfma_f32_16x16x128_f8f6f4 v[56:59], v[4:11], v[228:235], 0
	v_mfma_f32_16x16x128_f8f6f4 v[52:55], v[12:19], v[228:235], 0
	v_mfma_f32_16x16x128_f8f6f4 v[40:43], v[4:11], v[236:243], 0
	v_mfma_f32_16x16x128_f8f6f4 v[36:39], v[12:19], v[236:243], 0
.LCZ1_1_j:
	s_setprio 0
	s_barrier
	s_add_i32 s47, 0, 0x18000
	s_add_i32 s48, 0, 0x1c000
	ds_read_b128 v[4:7], v226 offset:32768
	ds_read_b128 v[8:11], v245 offset:32768
	ds_read_b128 v[12:15], v226 offset:34816
	ds_read_b128 v[16:19], v245 offset:34816
	ds_read_b128 v[20:23], v226 offset:49152
	ds_read_b128 v[24:27], v245 offset:49152
	ds_read_b128 v[28:31], v226 offset:51200
	ds_read_b128 v[32:35], v245 offset:51200
	s_add_u32 s20, s20, 0x130000
	s_addc_u32 s21, s21, 0
	s_mov_b32 m0, s29
	v_lshl_add_u64 v[164:165], s[20:21], 0, v[178:179]
	ds_read_b128 v[192:195], v227 offset:32768
	ds_read_b128 v[196:199], v246 offset:32768
	ds_read_b128 v[200:203], v227 offset:34816
	ds_read_b128 v[204:207], v246 offset:34816
	ds_read_b128 v[228:231], v227 offset:36864
	ds_read_b128 v[232:235], v246 offset:36864
	ds_read_b128 v[236:239], v227 offset:38912
	ds_read_b128 v[240:243], v246 offset:38912
	global_load_lds_dwordx4 v[164:165], off
	v_lshl_add_u64 v[164:165], s[20:21], 0, v[174:175]
	s_mov_b32 m0, s30
	s_nop 0
	global_load_lds_dwordx4 v[164:165], off
	s_waitcnt vmcnt(8)
	s_waitcnt lgkmcnt(0)
	s_barrier
	s_setprio 1
	v_mfma_f32_16x16x128_f8f6f4 v[160:163], v[4:11], v[192:199], v[160:163]
	v_mfma_f32_16x16x128_f8f6f4 v[156:159], v[12:19], v[192:199], v[156:159]
	v_mfma_f32_16x16x128_f8f6f4 v[144:147], v[4:11], v[200:207], v[144:147]
	v_mfma_f32_16x16x128_f8f6f4 v[140:143], v[12:19], v[200:207], v[140:143]
	v_mfma_f32_16x16x128_f8f6f4 v[128:131], v[4:11], v[228:235], v[128:131]
	v_mfma_f32_16x16x128_f8f6f4 v[124:127], v[12:19], v[228:235], v[124:127]
	v_mfma_f32_16x16x128_f8f6f4 v[112:115], v[4:11], v[236:243], v[112:115]
	v_mfma_f32_16x16x128_f8f6f4 v[108:111], v[12:19], v[236:243], v[108:111]
	v_mfma_f32_16x16x128_f8f6f4 v[152:155], v[20:27], v[192:199], v[152:155]
	v_mfma_f32_16x16x128_f8f6f4 v[148:151], v[28:35], v[192:199], v[148:151]
	v_mfma_f32_16x16x128_f8f6f4 v[136:139], v[20:27], v[200:207], v[136:139]
	v_mfma_f32_16x16x128_f8f6f4 v[132:135], v[28:35], v[200:207], v[132:135]
	v_mfma_f32_16x16x128_f8f6f4 v[120:123], v[20:27], v[228:235], v[120:123]
	v_mfma_f32_16x16x128_f8f6f4 v[116:119], v[28:35], v[228:235], v[116:119]
	v_mfma_f32_16x16x128_f8f6f4 v[104:107], v[20:27], v[236:243], v[104:107]
	v_mfma_f32_16x16x128_f8f6f4 v[100:103], v[28:35], v[236:243], v[100:103]
	s_setprio 0
	s_barrier
	s_add_i32 s20, s47, s26
	v_lshl_add_u64 v[164:165], v[184:185], 0, s[52:53]
	s_mov_b32 m0, s20
	ds_read_b128 v[192:195], v227 offset:49152
	ds_read_b128 v[196:199], v246 offset:49152
	ds_read_b128 v[200:203], v227 offset:51200
	ds_read_b128 v[204:207], v246 offset:51200
	ds_read_b128 v[228:231], v227 offset:53248
	ds_read_b128 v[232:235], v246 offset:53248
	ds_read_b128 v[236:239], v227 offset:55296
	ds_read_b128 v[240:243], v246 offset:55296
	global_load_lds_dwordx4 v[164:165], off
	s_add_i32 m0, s20, 0x2000
	s_add_u32 s18, s18, 0x20080
	v_lshl_add_u64 v[164:165], v[186:187], 0, s[52:53]
	s_addc_u32 s19, s19, 0
	s_add_i32 s20, s48, s26
	global_load_lds_dwordx4 v[164:165], off
	v_lshl_add_u64 v[164:165], s[18:19], 0, v[176:177]
	s_mov_b32 m0, s20
	s_nop 0
	global_load_lds_dwordx4 v[164:165], off
	v_lshl_add_u64 v[164:165], s[18:19], 0, v[172:173]
	s_add_i32 m0, s20, 0x2000
	s_nop 0
	global_load_lds_dwordx4 v[164:165], off
	v_lshl_add_u64 v[164:165], v[188:189], 0, s[52:53]
	s_mov_b32 m0, s38
	s_nop 0
	global_load_lds_dwordx4 v[164:165], off
	v_lshl_add_u64 v[164:165], v[190:191], 0, s[52:53]
	s_mov_b32 m0, s39
	s_nop 0
	global_load_lds_dwordx4 v[164:165], off
	s_waitcnt vmcnt(8)
	s_waitcnt lgkmcnt(0)
	s_barrier
	s_setprio 1
	v_mfma_f32_16x16x128_f8f6f4 v[96:99], v[4:11], v[192:199], v[96:99]
	v_mfma_f32_16x16x128_f8f6f4 v[92:95], v[12:19], v[192:199], v[92:95]
	v_mfma_f32_16x16x128_f8f6f4 v[80:83], v[4:11], v[200:207], v[80:83]
	v_mfma_f32_16x16x128_f8f6f4 v[76:79], v[12:19], v[200:207], v[76:79]
	v_mfma_f32_16x16x128_f8f6f4 v[64:67], v[4:11], v[228:235], v[64:67]
	v_mfma_f32_16x16x128_f8f6f4 v[60:63], v[12:19], v[228:235], v[60:63]
	v_mfma_f32_16x16x128_f8f6f4 v[48:51], v[4:11], v[236:243], v[48:51]
	v_mfma_f32_16x16x128_f8f6f4 v[44:47], v[12:19], v[236:243], v[44:47]
	v_mfma_f32_16x16x128_f8f6f4 v[88:91], v[20:27], v[192:199], v[88:91]
	v_mfma_f32_16x16x128_f8f6f4 v[84:87], v[28:35], v[192:199], v[84:87]
	v_mfma_f32_16x16x128_f8f6f4 v[72:75], v[20:27], v[200:207], v[72:75]
	v_mfma_f32_16x16x128_f8f6f4 v[68:71], v[28:35], v[200:207], v[68:71]
	v_mfma_f32_16x16x128_f8f6f4 v[56:59], v[20:27], v[228:235], v[56:59]
	v_mfma_f32_16x16x128_f8f6f4 v[52:55], v[28:35], v[228:235], v[52:55]
	v_mfma_f32_16x16x128_f8f6f4 v[40:43], v[20:27], v[236:243], v[40:43]
	v_mfma_f32_16x16x128_f8f6f4 v[36:39], v[28:35], v[236:243], v[36:39]
	s_setprio 0
	s_barrier
	s_add_i32 s46, s46, 2
	s_add_u32 s0, s0, 0x100
	s_addc_u32 s1, s1, 0
	s_add_u32 s44, s44, 0x100
	s_addc_u32 s45, s45, 0
	s_cmp_gt_u32 s46, 5
	s_cbranch_scc0 .LBB0_702
	s_and_b64 vcc, exec, s[10:11]
	s_cbranch_vccz .LBB0_705
	s_barrier

.LBB0_878:
	v_lshlrev_b32_e32 v4, 10, v170
	v_and_b32_e32 v4, 0x3fffc00, v4
	v_add_u32_e32 v178, v4, v1
	v_bfe_u32 v4, v170, 16, 16
	s_add_u32 s63, s34, 0x100
	v_mov_b32_e32 v36, 0
	v_lshl_add_u32 v180, v4, 10, v1
	v_mov_b32_e32 v181, v2
	v_mov_b32_e32 v179, v2
	s_addc_u32 s64, s35, 0
	s_mov_b32 s65, -2
	s_mov_b64 s[34:35], s[24:25]
	s_mov_b64 s[70:71], 0x80
.LBB0_879:
	s_add_u32 s38, s34, 0x80
	s_addc_u32 s39, s35, 0
	s_add_i32 s66, 0, 0x10000
	s_cmp_eq_u32 s65, 4
	s_cselect_b64 vcc, -1, 0
	s_and_b64 s[36:37], vcc, exec
	s_cselect_b32 s39, s1, s39
	s_cselect_b32 s38, s0, s38
	s_cselect_b32 s37, s29, s64
	s_cselect_b32 s36, s28, s63
	s_add_i32 s67, 0, 0x14000
	ds_read_b128 v[20:23], v192
	ds_read_b128 v[24:27], v207
	ds_read_b128 v[28:31], v192 offset:2048
	ds_read_b128 v[32:35], v207 offset:2048
	ds_read_b128 v[4:7], v192 offset:16384
	ds_read_b128 v[8:11], v207 offset:16384
	ds_read_b128 v[12:15], v192 offset:18432
	ds_read_b128 v[16:19], v207 offset:18432
	v_lshl_add_u64 v[164:165], s[34:35], 0, v[178:179]
	s_add_i32 m0, s47, 0xc000
	ds_read_b128 v[182:185], v193
	ds_read_b128 v[186:189], v208
	ds_read_b128 v[198:201], v193 offset:2048
	ds_read_b128 v[202:205], v208 offset:2048
	ds_read_b128 v[226:229], v193 offset:4096
	ds_read_b128 v[230:233], v208 offset:4096
	ds_read_b128 v[234:237], v193 offset:6144
	ds_read_b128 v[238:241], v208 offset:6144
	global_load_lds_dwordx4 v[164:165], off
	v_lshl_add_u64 v[164:165], s[34:35], 0, v[180:181]
	s_add_i32 m0, s47, 0xe000
	s_nop 0
	global_load_lds_dwordx4 v[164:165], off
	s_waitcnt vmcnt(8)
	s_waitcnt lgkmcnt(0)
	s_barrier
	s_setprio 1
	s_cmp_eq_u32 s65, -2
	s_cbranch_scc1 .LCZ2_0_z
	v_mfma_f32_16x16x128_f8f6f4 v[160:163], v[20:27], v[182:189], v[160:163]
	v_mfma_f32_16x16x128_f8f6f4 v[156:159], v[28:35], v[182:189], v[156:159]
	v_mfma_f32_16x16x128_f8f6f4 v[144:147], v[20:27], v[198:205], v[144:147]
	v_mfma_f32_16x16x128_f8f6f4 v[140:143], v[28:35], v[198:205], v[140:143]
	v_mfma_f32_16x16x128_f8f6f4 v[128:131], v[20:27], v[226:233], v[128:131]
	v_mfma_f32_16x16x128_f8f6f4 v[124:127], v[28:35], v[226:233], v[124:127]
	v_mfma_f32_16x16x128_f8f6f4 v[112:115], v[20:27], v[234:241], v[112:115]
	v_mfma_f32_16x16x128_f8f6f4 v[108:111], v[28:35], v[234:241], v[108:111]
	v_mfma_f32_16x16x128_f8f6f4 v[152:155], v[4:11], v[182:189], v[152:155]
	v_mfma_f32_16x16x128_f8f6f4 v[148:151], v[12:19], v[182:189], v[148:151]
	v_mfma_f32_16x16x128_f8f6f4 v[136:139], v[4:11], v[198:205], v[136:139]
	v_mfma_f32_16x16x128_f8f6f4 v[132:135], v[12:19], v[198:205], v[132:135]
	v_mfma_f32_16x16x128_f8f6f4 v[120:123], v[4:11], v[226:233], v[120:123]
	v_mfma_f32_16x16x128_f8f6f4 v[116:119], v[12:19], v[226:233], v[116:119]
	v_mfma_f32_16x16x128_f8f6f4 v[104:107], v[4:11], v[234:241], v[104:107]
	v_mfma_f32_16x16x128_f8f6f4 v[100:103], v[12:19], v[234:241], v[100:103]
	s_branch .LCZ2_0_j
.LCZ2_0_z:
	v_mfma_f32_16x16x128_f8f6f4 v[160:163], v[20:27], v[182:189], 0
	v_mfma_f32_16x16x128_f8f6f4 v[156:159], v[28:35], v[182:189], 0
	v_mfma_f32_16x16x128_f8f6f4 v[144:147], v[20:27], v[198:205], 0
	v_mfma_f32_16x16x128_f8f6f4 v[140:143], v[28:35], v[198:205], 0
	v_mfma_f32_16x16x128_f8f6f4 v[128:131], v[20:27], v[226:233], 0
	v_mfma_f32_16x16x128_f8f6f4 v[124:127], v[28:35], v[226:233], 0
	v_mfma_f32_16x16x128_f8f6f4 v[112:115], v[20:27], v[234:241], 0
	v_mfma_f32_16x16x128_f8f6f4 v[108:111], v[28:35], v[234:241], 0
	v_mfma_f32_16x16x128_f8f6f4 v[152:155], v[4:11], v[182:189], 0
	v_mfma_f32_16x16x128_f8f6f4 v[148:151], v[12:19], v[182:189], 0
	v_mfma_f32_16x16x128_f8f6f4 v[136:139], v[4:11], v[198:205], 0
	v_mfma_f32_16x16x128_f8f6f4 v[132:135], v[12:19], v[198:205], 0
	v_mfma_f32_16x16x128_f8f6f4 v[120:123], v[4:11], v[226:233], 0
	v_mfma_f32_16x16x128_f8f6f4 v[116:119], v[12:19], v[226:233], 0
	v_mfma_f32_16x16x128_f8f6f4 v[104:107], v[4:11], v[234:241], 0
	v_mfma_f32_16x16x128_f8f6f4 v[100:103], v[12:19], v[234:241], 0
.LCZ2_0_j:
	s_setprio 0
	s_barrier
	s_add_i32 s66, s66, s46
	v_lshl_add_u64 v[182:183], s[36:37], 0, v[176:177]
	s_mov_b32 m0, s66
	ds_read_b128 v[198:201], v193 offset:16384
	ds_read_b128 v[202:205], v208 offset:16384
	ds_read_b128 v[226:229], v193 offset:18432
	ds_read_b128 v[230:233], v208 offset:18432
	ds_read_b128 v[234:237], v193 offset:20480
	ds_read_b128 v[238:241], v208 offset:20480
	ds_read_b128 v[242:245], v193 offset:22528
	ds_read_b128 v[246:249], v208 offset:22528
	global_load_lds_dwordx4 v[182:183], off
	s_add_i32 m0, s66, 0x2000
	s_add_u32 s68, s36, 0x20000
	v_lshl_add_u64 v[184:185], s[36:37], 0, v[174:175]
	s_addc_u32 s69, s37, 0
	s_add_i32 s66, s67, s46
	global_load_lds_dwordx4 v[184:185], off
	v_lshl_add_u64 v[164:165], s[68:69], 0, v[176:177]
	s_mov_b32 m0, s66
	v_mov_b32_e32 v167, v2
	global_load_lds_dwordx4 v[164:165], off
	v_lshl_add_u64 v[164:165], s[68:69], 0, v[174:175]
	s_add_i32 m0, s66, 0x2000
	s_nop 0
	global_load_lds_dwordx4 v[164:165], off
	v_cndmask_b32_e32 v165, v196, v194, vcc
	v_lshlrev_b32_e32 v164, 10, v165
	v_and_b32_e32 v164, 0x3fffc00, v164
	v_add_u32_e32 v164, v164, v1
	s_mov_b32 m0, s47
	v_bfe_u32 v165, v165, 16, 16
	global_load_lds_dwordx4 v164, s[38:39]
	v_lshl_add_u32 v166, v165, 10, v1
	s_mov_b32 m0, s48
	v_mov_b32_e32 v165, v2
	global_load_lds_dwordx4 v166, s[38:39]
	s_waitcnt vmcnt(8)
	s_waitcnt lgkmcnt(0)
	v_lshl_add_u64 v[188:189], s[38:39], 0, v[164:165]
	v_lshl_add_u64 v[186:187], s[38:39], 0, v[166:167]
	s_barrier
	s_setprio 1
	s_cmp_eq_u32 s65, -2
	s_cbranch_scc1 .LCZ2_1_z
	v_mfma_f32_16x16x128_f8f6f4 v[96:99], v[20:27], v[198:205], v[96:99]
	v_mfma_f32_16x16x128_f8f6f4 v[92:95], v[28:35], v[198:205], v[92:95]
	v_mfma_f32_16x16x128_f8f6f4 v[80:83], v[20:27], v[226:233], v[80:83]
	v_mfma_f32_16x16x128_f8f6f4 v[76:79], v[28:35], v[226:233], v[76:79]
	v_mfma_f32_16x16x128_f8f6f4 v[64:67], v[20:27], v[234:241], v[64:67]
	v_mfma_f32_16x16x128_f8f6f4 v[60:63], v[28:35], v[234:241], v[60:63]
	v_mfma_f32_16x16x128_f8f6f4 v[48:51], v[20:27], v[242:249], v[48:51]
	v_mfma_f32_16x16x128_f8f6f4 v[44:47], v[28:35], v[242:249], v[44:47]
	v_mfma_f32_16x16x128_f8f6f4 v[88:91], v[4:11], v[198:205], v[88:91]
	v_mfma_f32_16x16x128_f8f6f4 v[84:87], v[12:19], v[198:205], v[84:87]
	v_mfma_f32_16x16x128_f8f6f4 v[72:75], v[4:11], v[226:233], v[72:75]
	v_mfma_f32_16x16x128_f8f6f4 v[68:71], v[12:19], v[226:233], v[68:71]
	v_mfma_f32_16x16x128_f8f6f4 v[56:59], v[4:11], v[234:241], v[56:59]
	v_mfma_f32_16x16x128_f8f6f4 v[52:55], v[12:19], v[234:241], v[52:55]
	v_mfma_f32_16x16x128_f8f6f4 v[40:43], v[4:11], v[242:249], v[40:43]
	v_mfma_f32_16x16x128_f8f6f4 v[36:39], v[12:19], v[242:249], v[36:39]
	s_branch .LCZ2_1_j
.LCZ2_1_z:
	v_mfma_f32_16x16x128_f8f6f4 v[96:99], v[20:27], v[198:205], 0
	v_mfma_f32_16x16x128_f8f6f4 v[92:95], v[28:35], v[198:205], 0
	v_mfma_f32_16x16x128_f8f6f4 v[80:83], v[20:27], v[226:233], 0
	v_mfma_f32_16x16x128_f8f6f4 v[76:79], v[28:35], v[226:233], 0
	v_mfma_f32_16x16x128_f8f6f4 v[64:67], v[20:27], v[234:241], 0
	v_mfma_f32_16x16x128_f8f6f4 v[60:63], v[28:35], v[234:241], 0
	v_mfma_f32_16x16x128_f8f6f4 v[48:51], v[20:27], v[242:249], 0
	v_mfma_f32_16x16x128_f8f6f4 v[44:47], v[28:35], v[242:249], 0
	v_mfma_f32_16x16x128_f8f6f4 v[88:91], v[4:11], v[198:205], 0
	v_mfma_f32_16x16x128_f8f6f4 v[84:87], v[12:19], v[198:205], 0
	v_mfma_f32_16x16x128_f8f6f4 v[72:75], v[4:11], v[226:233], 0
	v_mfma_f32_16x16x128_f8f6f4 v[68:71], v[12:19], v[226:233], 0
	v_mfma_f32_16x16x128_f8f6f4 v[56:59], v[4:11], v[234:241], 0
	v_mfma_f32_16x16x128_f8f6f4 v[52:55], v[12:19], v[234:241], 0
	v_mfma_f32_16x16x128_f8f6f4 v[40:43], v[4:11], v[242:249], 0
	v_mfma_f32_16x16x128_f8f6f4 v[36:39], v[12:19], v[242:249], 0
.LCZ2_1_j:
	s_setprio 0
	s_barrier
	s_add_i32 s66, 0, 0x18000
	s_add_i32 s67, 0, 0x1c000
	ds_read_b128 v[4:7], v192 offset:32768
	ds_read_b128 v[8:11], v207 offset:32768
	ds_read_b128 v[12:15], v192 offset:34816
	ds_read_b128 v[16:19], v207 offset:34816
	ds_read_b128 v[20:23], v192 offset:49152
	ds_read_b128 v[24:27], v207 offset:49152
	ds_read_b128 v[28:31], v192 offset:51200
	ds_read_b128 v[32:35], v207 offset:51200
	v_cndmask_b32_e32 v164, v170, v195, vcc
	v_lshlrev_b32_e32 v165, 10, v164
	v_and_b32_e32 v165, 0x3fffc00, v165
	s_mov_b32 m0, s49
	v_add_u32_e32 v165, v165, v1
	v_bfe_u32 v164, v164, 16, 16
	ds_read_b128 v[198:201], v193 offset:32768
	ds_read_b128 v[202:205], v208 offset:32768
	ds_read_b128 v[226:229], v193 offset:34816
	ds_read_b128 v[230:233], v208 offset:34816
	ds_read_b128 v[234:237], v193 offset:36864
	ds_read_b128 v[238:241], v208 offset:36864
	ds_read_b128 v[242:245], v193 offset:38912
	ds_read_b128 v[246:249], v208 offset:38912
	global_load_lds_dwordx4 v165, s[38:39]
	v_lshl_add_u32 v164, v164, 10, v1
	s_mov_b32 m0, s50
	s_nop 0
	global_load_lds_dwordx4 v164, s[38:39]
	s_waitcnt vmcnt(8)
	s_waitcnt lgkmcnt(0)
	s_barrier
	s_setprio 1
	v_mfma_f32_16x16x128_f8f6f4 v[160:163], v[4:11], v[198:205], v[160:163]
	v_mfma_f32_16x16x128_f8f6f4 v[156:159], v[12:19], v[198:205], v[156:159]
	v_mfma_f32_16x16x128_f8f6f4 v[144:147], v[4:11], v[226:233], v[144:147]
	v_mfma_f32_16x16x128_f8f6f4 v[140:143], v[12:19], v[226:233], v[140:143]
	v_mfma_f32_16x16x128_f8f6f4 v[128:131], v[4:11], v[234:241], v[128:131]
	v_mfma_f32_16x16x128_f8f6f4 v[124:127], v[12:19], v[234:241], v[124:127]
	v_mfma_f32_16x16x128_f8f6f4 v[112:115], v[4:11], v[242:249], v[112:115]
	v_mfma_f32_16x16x128_f8f6f4 v[108:111], v[12:19], v[242:249], v[108:111]
	v_mfma_f32_16x16x128_f8f6f4 v[152:155], v[20:27], v[198:205], v[152:155]
	v_mfma_f32_16x16x128_f8f6f4 v[148:151], v[28:35], v[198:205], v[148:151]
	v_mfma_f32_16x16x128_f8f6f4 v[136:139], v[20:27], v[226:233], v[136:139]
	v_mfma_f32_16x16x128_f8f6f4 v[132:135], v[28:35], v[226:233], v[132:135]
	v_mfma_f32_16x16x128_f8f6f4 v[120:123], v[20:27], v[234:241], v[120:123]
	v_mfma_f32_16x16x128_f8f6f4 v[116:119], v[28:35], v[234:241], v[116:119]
	v_mfma_f32_16x16x128_f8f6f4 v[104:107], v[20:27], v[242:249], v[104:107]
	v_mfma_f32_16x16x128_f8f6f4 v[100:103], v[28:35], v[242:249], v[100:103]
	s_setprio 0
	s_barrier
	s_add_i32 s38, s66, s46
	v_lshl_add_u64 v[164:165], v[182:183], 0, s[70:71]
	s_mov_b32 m0, s38
	ds_read_b128 v[198:201], v193 offset:49152
	ds_read_b128 v[202:205], v208 offset:49152
	ds_read_b128 v[226:229], v193 offset:51200
	ds_read_b128 v[230:233], v208 offset:51200
	ds_read_b128 v[234:237], v193 offset:53248
	ds_read_b128 v[238:241], v208 offset:53248
	ds_read_b128 v[242:245], v193 offset:55296
	ds_read_b128 v[246:249], v208 offset:55296
	global_load_lds_dwordx4 v[164:165], off
	s_add_i32 m0, s38, 0x2000
	s_add_u32 s36, s36, 0x20080
	v_lshl_add_u64 v[164:165], v[184:185], 0, s[70:71]
	s_addc_u32 s37, s37, 0
	s_add_i32 s38, s67, s46
	global_load_lds_dwordx4 v[164:165], off
	v_lshl_add_u64 v[164:165], s[36:37], 0, v[176:177]
	s_mov_b32 m0, s38
	s_nop 0
	global_load_lds_dwordx4 v[164:165], off
	v_lshl_add_u64 v[164:165], s[36:37], 0, v[174:175]
	s_add_i32 m0, s38, 0x2000
	s_nop 0
	global_load_lds_dwordx4 v[164:165], off
	v_lshl_add_u64 v[164:165], v[188:189], 0, s[70:71]
	s_mov_b32 m0, s55
	s_nop 0
	global_load_lds_dwordx4 v[164:165], off
	v_lshl_add_u64 v[164:165], v[186:187], 0, s[70:71]
	s_mov_b32 m0, s56
	s_nop 0
	global_load_lds_dwordx4 v[164:165], off
	s_waitcnt vmcnt(8)
	s_waitcnt lgkmcnt(0)
	s_barrier
	s_setprio 1
	v_mfma_f32_16x16x128_f8f6f4 v[96:99], v[4:11], v[198:205], v[96:99]
	v_mfma_f32_16x16x128_f8f6f4 v[92:95], v[12:19], v[198:205], v[92:95]
	v_mfma_f32_16x16x128_f8f6f4 v[80:83], v[4:11], v[226:233], v[80:83]
	v_mfma_f32_16x16x128_f8f6f4 v[76:79], v[12:19], v[226:233], v[76:79]
	v_mfma_f32_16x16x128_f8f6f4 v[64:67], v[4:11], v[234:241], v[64:67]
	v_mfma_f32_16x16x128_f8f6f4 v[60:63], v[12:19], v[234:241], v[60:63]
	v_mfma_f32_16x16x128_f8f6f4 v[48:51], v[4:11], v[242:249], v[48:51]
	v_mfma_f32_16x16x128_f8f6f4 v[44:47], v[12:19], v[242:249], v[44:47]
	v_mfma_f32_16x16x128_f8f6f4 v[88:91], v[20:27], v[198:205], v[88:91]
	v_mfma_f32_16x16x128_f8f6f4 v[84:87], v[28:35], v[198:205], v[84:87]
	v_mfma_f32_16x16x128_f8f6f4 v[72:75], v[20:27], v[226:233], v[72:75]
	v_mfma_f32_16x16x128_f8f6f4 v[68:71], v[28:35], v[226:233], v[68:71]
	v_mfma_f32_16x16x128_f8f6f4 v[56:59], v[20:27], v[234:241], v[56:59]
	v_mfma_f32_16x16x128_f8f6f4 v[52:55], v[28:35], v[234:241], v[52:55]
	v_mfma_f32_16x16x128_f8f6f4 v[40:43], v[20:27], v[242:249], v[40:43]
	v_mfma_f32_16x16x128_f8f6f4 v[36:39], v[28:35], v[242:249], v[36:39]
	s_setprio 0
	s_barrier
	s_add_i32 s65, s65, 2
	s_add_u32 s34, s34, 0x100
	s_addc_u32 s35, s35, 0
	s_add_u32 s63, s63, 0x100
	s_addc_u32 s64, s64, 0
	s_cmp_gt_u32 s65, 5
	s_cbranch_scc0 .LBB0_879
	s_and_b64 vcc, exec, s[26:27]
	s_cbranch_vccz .LBB0_882
	s_barrier
